# baseline (speedup 1.0000x reference)
.Lstore:
	s_sleep 30
	s_and_saveexec_b64 s[2:3], vcc
	s_cbranch_execz .Ldog_main_done
	global_store_dword v5, v164, s[26:27]
